# speedup vs baseline: 1.0447x; 1.0447x over previous
_Z19gemm_scatter_kernelPKfPKDF16_S0_PDF16_S3_PfPjPKiS7_S7_S7_S7_PiS5_:
	s_mov_b32 s44, 0
	s_load_dwordx4 s[24:27], s[0:1], 0x0
	s_load_dwordx2 s[4:5], s[0:1], 0x10
	s_ashr_i32 s3, s2, 31
	s_lshr_b32 s3, s3, 25
	s_add_i32 s3, s2, s3
	s_ashr_i32 s14, s3, 7
	s_and_b32 s3, s3, 0xffffff80
	s_movk_i32 s6, 0x100
	s_sub_i32 s3, s2, s3
	v_cmp_gt_u32_e64 s[8:9], s6, v0
	v_mov_b32_e32 v147, 0
	v_lshlrev_b32_e32 v10, 4, v0
	v_mov_b32_e32 v150, 0
	s_and_saveexec_b64 s[6:7], s[8:9]
	s_cbranch_execz .LBB1_2
	s_load_dwordx2 s[12:13], s[0:1], 0x58
	s_ashr_i32 s15, s14, 31
	s_lshl_b64 s[16:17], s[14:15], 16
	v_mov_b32_e32 v11, 0
	s_movk_i32 s10, 0x2000
	s_waitcnt lgkmcnt(0)
	s_add_u32 s12, s12, s16
	s_addc_u32 s13, s13, s17
	v_lshl_add_u64 v[2:3], s[12:13], 0, v[10:11]
	v_add_co_u32_e32 v4, vcc, s10, v2
	s_movk_i32 s10, 0x4000
	s_nop 0
	v_addc_co_u32_e32 v5, vcc, 0, v3, vcc
	v_add_co_u32_e32 v6, vcc, s10, v2
	s_movk_i32 s10, 0x6000
	s_nop 0
	v_addc_co_u32_e32 v7, vcc, 0, v3, vcc
	global_load_dwordx4 v[142:145], v10, s[12:13]
	global_load_dwordx4 v[138:141], v[4:5], off offset:-4096
	global_load_dwordx4 v[134:137], v[4:5], off
	global_load_dwordx4 v[130:133], v[6:7], off offset:-4096
	v_add_co_u32_e32 v4, vcc, s10, v2
	s_mov_b32 s10, 0x8000
	s_nop 0
	v_addc_co_u32_e32 v5, vcc, 0, v3, vcc
	global_load_dwordx4 v[126:129], v[6:7], off
	global_load_dwordx4 v[122:125], v[4:5], off offset:-4096
	v_add_co_u32_e32 v6, vcc, s10, v2
	s_mov_b32 s10, 0xa000
	s_nop 0
	v_addc_co_u32_e32 v7, vcc, 0, v3, vcc
	global_load_dwordx4 v[118:121], v[4:5], off
	global_load_dwordx4 v[114:117], v[6:7], off offset:-4096
	v_add_co_u32_e32 v4, vcc, s10, v2
	s_mov_b32 s10, 0xc000
	s_nop 0
	v_addc_co_u32_e32 v5, vcc, 0, v3, vcc
	global_load_dwordx4 v[110:113], v[6:7], off
	global_load_dwordx4 v[106:109], v[4:5], off offset:-4096
	v_add_co_u32_e32 v6, vcc, s10, v2
	s_mov_b32 s10, 0xe000
	s_nop 0
	v_addc_co_u32_e32 v7, vcc, 0, v3, vcc
	global_load_dwordx4 v[102:105], v[4:5], off
	global_load_dwordx4 v[98:101], v[6:7], off offset:-4096
	v_add_co_u32_e32 v4, vcc, s10, v2
	s_ashr_i32 s12, s3, 3
	s_nop 0
	v_addc_co_u32_e32 v5, vcc, 0, v3, vcc
	s_mov_b32 s10, 0xf000
	s_ashr_i32 s13, s12, 31
	global_load_dwordx4 v[94:97], v[6:7], off
	global_load_dwordx4 v[90:93], v[4:5], off offset:-4096
	v_add_co_u32_e32 v6, vcc, s10, v2
	s_and_b32 s10, s3, 7
	s_lshl_b64 s[12:13], s[12:13], 12
	s_mov_b32 s11, 0
	v_addc_co_u32_e32 v7, vcc, 0, v3, vcc
	v_lshl_add_u64 v[2:3], v[2:3], 0, s[12:13]
	s_lshl_b32 s10, s10, 1
	v_lshl_add_u64 v[2:3], v[2:3], 0, s[10:11]
	global_load_dwordx4 v[82:85], v[6:7], off
	global_load_ushort v1, v[2:3], off
	global_load_dwordx4 v[86:89], v[4:5], off
	s_waitcnt vmcnt(1)
	v_and_b32_e32 v150, 0xffff, v1

.LBB1_47:
	s_cmp_eq_u32 s36, 2
	s_cbranch_scc0 .LBB1_36
	s_cmp_eq_u32 s38, s35
	s_cbranch_scc1 .LBB1_36
	s_mul_i32 s40, s14, 0x30d400
	s_mul_hi_i32 s41, s14, 0x30d400
	s_add_u32 s40, s26, s40
	s_addc_u32 s41, s27, s41
	v_add_u32_e32 v230, 0x1c5c0, v142
	v_add_u32_e32 v231, 0x16400, v142
	ds_read_b32 v232, v230
	ds_read_b32 v238, v231
	ds_read_b32 v233, v230 offset:2048
	ds_read_b32 v239, v231 offset:2048
	ds_read_b32 v234, v230 offset:4096
	ds_read_b32 v240, v231 offset:4096
	ds_read_b32 v235, v230 offset:6144
	ds_read_b32 v241, v231 offset:6144
	ds_read_b32 v236, v230 offset:8192
	ds_read_b32 v242, v231 offset:8192
	ds_read_b32 v237, v230 offset:10240
	ds_read_b32 v243, v231 offset:10240
	s_waitcnt lgkmcnt(0)
	v_lshlrev_b32_e32 v232, 2, v232
	v_lshlrev_b32_e32 v233, 2, v233
	v_lshlrev_b32_e32 v234, 2, v234
	v_lshlrev_b32_e32 v235, 2, v235
	v_lshlrev_b32_e32 v236, 2, v236
	v_lshlrev_b32_e32 v237, 2, v237
	global_store_dword v232, v238, s[40:41]
	global_store_dword v233, v239, s[40:41]
	global_store_dword v234, v240, s[40:41]
	global_store_dword v235, v241, s[40:41]
	global_store_dword v236, v242, s[40:41]
	global_store_dword v237, v243, s[40:41]
	ds_read_b32 v244, v230 offset:12288
	ds_read_b32 v250, v231 offset:12288
	ds_read_b32 v245, v230 offset:14336
	ds_read_b32 v251, v231 offset:14336
	ds_read_b32 v246, v230 offset:16384
	ds_read_b32 v252, v231 offset:16384
	ds_read_b32 v247, v230 offset:18432
	ds_read_b32 v253, v231 offset:18432
	ds_read_b32 v248, v230 offset:20480
	ds_read_b32 v254, v231 offset:20480
	ds_read_b32 v249, v230 offset:22528
	ds_read_b32 v255, v231 offset:22528
	ds_read_b32 v230, v230 offset:24576
	ds_read_b32 v231, v231 offset:24576
	s_waitcnt lgkmcnt(0)
	v_lshlrev_b32_e32 v244, 2, v244
	v_lshlrev_b32_e32 v245, 2, v245
	v_lshlrev_b32_e32 v246, 2, v246
	v_lshlrev_b32_e32 v247, 2, v247
	v_lshlrev_b32_e32 v248, 2, v248
	v_lshlrev_b32_e32 v249, 2, v249
	global_store_dword v244, v250, s[40:41]
	global_store_dword v245, v251, s[40:41]
	global_store_dword v246, v252, s[40:41]
	global_store_dword v247, v253, s[40:41]
	global_store_dword v248, v254, s[40:41]
	global_store_dword v249, v255, s[40:41]
	v_lshlrev_b32_e32 v230, 2, v230
	s_movk_i32 s45, 0x6a
	v_cmp_gt_u32_e64 s[46:47], s45, v0
	s_and_saveexec_b64 s[42:43], s[46:47]
	global_store_dword v230, v231, s[40:41]
	s_mov_b64 exec, s[42:43]
	s_mov_b32 s44, 1
	s_branch .LBB1_36

.LBB1_62:
	s_or_b64 exec, exec, s[0:1]
	v_add_u32_e32 v1, 0x1c5c0, v142
	s_waitcnt lgkmcnt(0)
	s_barrier
	s_cmp_eq_u32 s44, 0
	s_cbranch_scc0 .LBB1_66
	s_waitcnt vmcnt(3)
	ds_read2st64_b32 v[4:5], v1 offset1:8
	v_add_u32_e32 v2, 0x16400, v142
	s_waitcnt vmcnt(2)
	ds_read2st64_b32 v[6:7], v2 offset1:8
	s_mul_i32 s0, s14, 0x30d400
	s_mul_hi_i32 s1, s14, 0x30d400
	s_add_u32 s0, s26, s0
	s_addc_u32 s1, s27, s1
	s_waitcnt lgkmcnt(1)
	v_ashrrev_i32_e32 v9, 31, v4
	v_mov_b32_e32 v8, v4
	v_lshl_add_u64 v[8:9], v[8:9], 2, s[0:1]
	s_waitcnt lgkmcnt(0)
	global_store_dword v[8:9], v6, off
	v_ashrrev_i32_e32 v9, 31, v5
	v_mov_b32_e32 v8, v5
	v_lshl_add_u64 v[4:5], v[8:9], 2, s[0:1]
	global_store_dword v[4:5], v7, off
	ds_read2st64_b32 v[4:5], v1 offset0:24 offset1:40
	v_add_u32_e32 v3, 0x17400, v142
	v_add_u32_e32 v6, 0x1d5c0, v142
	v_add_u32_e32 v8, 0x1e5c0, v142
	v_add_u32_e32 v10, 0x1f5c0, v142
	v_add_u32_e32 v12, 0x205c0, v142
	v_add_u32_e32 v7, 0x18400, v142
	v_add_u32_e32 v9, 0x19400, v142
	v_add_u32_e32 v11, 0x1a400, v142
	ds_read_b32 v3, v3
	ds_read_b32 v6, v6
	ds_read_b32 v13, v7
	ds_read_b32 v8, v8
	ds_read_b32 v16, v9
	ds_read_b32 v10, v10
	ds_read_b32 v17, v11
	ds_read_b32 v12, v12
	ds_read2st64_b32 v[14:15], v2 offset0:24 offset1:40
	s_waitcnt lgkmcnt(7)
	v_ashrrev_i32_e32 v7, 31, v6
	v_lshl_add_u64 v[6:7], v[6:7], 2, s[0:1]
	global_store_dword v[6:7], v3, off
	v_ashrrev_i32_e32 v7, 31, v4
	v_mov_b32_e32 v6, v4
	v_lshl_add_u64 v[6:7], v[6:7], 2, s[0:1]
	s_waitcnt lgkmcnt(5)
	v_ashrrev_i32_e32 v9, 31, v8
	s_waitcnt lgkmcnt(0)
	global_store_dword v[6:7], v14, off
	v_lshl_add_u64 v[6:7], v[8:9], 2, s[0:1]
	global_store_dword v[6:7], v13, off
	v_ashrrev_i32_e32 v7, 31, v5
	v_mov_b32_e32 v6, v5
	v_lshl_add_u64 v[4:5], v[6:7], 2, s[0:1]
	global_store_dword v[4:5], v15, off
	ds_read2st64_b32 v[4:5], v1 offset0:56 offset1:72
	ds_read2st64_b32 v[8:9], v2 offset0:56 offset1:72
	v_ashrrev_i32_e32 v11, 31, v10
	v_lshl_add_u64 v[6:7], v[10:11], 2, s[0:1]
	global_store_dword v[6:7], v16, off
	s_waitcnt lgkmcnt(1)
	v_ashrrev_i32_e32 v7, 31, v4
	v_mov_b32_e32 v6, v4
	v_lshl_add_u64 v[6:7], v[6:7], 2, s[0:1]
	v_ashrrev_i32_e32 v13, 31, v12
	s_waitcnt lgkmcnt(0)
	global_store_dword v[6:7], v8, off
	v_lshl_add_u64 v[6:7], v[12:13], 2, s[0:1]
	global_store_dword v[6:7], v17, off
	v_add_u32_e32 v3, 0x1b400, v142
	v_add_u32_e32 v4, 0x215c0, v142
	ds_read_b32 v3, v3
	ds_read_b32 v4, v4
	v_ashrrev_i32_e32 v7, 31, v5
	v_mov_b32_e32 v6, v5
	s_movk_i32 s2, 0x26a
	v_lshl_add_u64 v[6:7], v[6:7], 2, s[0:1]
	s_waitcnt lgkmcnt(0)
	v_ashrrev_i32_e32 v5, 31, v4
	v_lshl_add_u64 v[4:5], v[4:5], 2, s[0:1]
	v_cmp_gt_u32_e32 vcc, s2, v0
	global_store_dword v[6:7], v9, off
	global_store_dword v[4:5], v3, off
	s_and_saveexec_b64 s[2:3], vcc
	s_cbranch_execz .LBB1_64
	ds_read_b32 v4, v1 offset:22528
	ds_read_b32 v1, v2 offset:22528
	s_waitcnt lgkmcnt(1)
	v_ashrrev_i32_e32 v5, 31, v4
	v_lshl_add_u64 v[2:3], v[4:5], 2, s[0:1]
	s_waitcnt lgkmcnt(0)
	global_store_dword v[2:3], v1, off

	.amdhsa_kernel _Z19gemm_scatter_kernelPKfPKDF16_S0_PDF16_S3_PfPjPKiS7_S7_S7_S7_PiS5_
		.amdhsa_group_segment_fixed_size 144320
		.amdhsa_private_segment_fixed_size 0
		.amdhsa_kernarg_size 112
		.amdhsa_user_sgpr_count 2
		.amdhsa_user_sgpr_dispatch_ptr 0
		.amdhsa_user_sgpr_queue_ptr 0
		.amdhsa_user_sgpr_kernarg_segment_ptr 1
		.amdhsa_user_sgpr_dispatch_id 0
		.amdhsa_user_sgpr_kernarg_preload_length 0
		.amdhsa_user_sgpr_kernarg_preload_offset 0
		.amdhsa_user_sgpr_private_segment_size 0
		.amdhsa_uses_dynamic_stack 0
		.amdhsa_enable_private_segment 0
		.amdhsa_system_sgpr_workgroup_id_x 1
		.amdhsa_system_sgpr_workgroup_id_y 0
		.amdhsa_system_sgpr_workgroup_id_z 0
		.amdhsa_system_sgpr_workgroup_info 0
		.amdhsa_system_vgpr_workitem_id 0
		.amdhsa_next_free_vgpr 256
		.amdhsa_next_free_sgpr 96
		.amdhsa_accum_offset 256
		.amdhsa_reserve_vcc 1
		.amdhsa_float_round_mode_32 0
		.amdhsa_float_round_mode_16_64 0
		.amdhsa_float_denorm_mode_32 3
		.amdhsa_float_denorm_mode_16_64 3
		.amdhsa_dx10_clamp 1
		.amdhsa_ieee_mode 1
		.amdhsa_fp16_overflow 0
		.amdhsa_tg_split 0
		.amdhsa_exception_fp_ieee_invalid_op 0
		.amdhsa_exception_fp_denorm_src 0
		.amdhsa_exception_fp_ieee_div_zero 0
		.amdhsa_exception_fp_ieee_overflow 0
		.amdhsa_exception_fp_ieee_underflow 0
		.amdhsa_exception_fp_ieee_inexact 0
		.amdhsa_exception_int_div_zero 0
	.end_amdhsa_kernel

amdhsa.kernels:
  - .agpr_count:     0
    .args:
      - .actual_access:  read_only
        .address_space:  global
        .offset:         0
        .size:           8
        .value_kind:     global_buffer
      - .actual_access:  read_only
        .address_space:  global
        .offset:         8
        .size:           8
        .value_kind:     global_buffer
      - .actual_access:  read_only
        .address_space:  global
        .offset:         16
        .size:           8
        .value_kind:     global_buffer
      - .actual_access:  read_only
        .address_space:  global
        .offset:         24
        .size:           8
        .value_kind:     global_buffer
      - .actual_access:  read_only
        .address_space:  global
        .offset:         32
        .size:           8
        .value_kind:     global_buffer
      - .actual_access:  read_only
        .address_space:  global
        .offset:         40
        .size:           8
        .value_kind:     global_buffer
      - .actual_access:  read_only
        .address_space:  global
        .offset:         48
        .size:           8
        .value_kind:     global_buffer
      - .actual_access:  write_only
        .address_space:  global
        .offset:         56
        .size:           8
        .value_kind:     global_buffer
      - .actual_access:  write_only
        .address_space:  global
        .offset:         64
        .size:           8
        .value_kind:     global_buffer
      - .actual_access:  write_only
        .address_space:  global
        .offset:         72
        .size:           8
        .value_kind:     global_buffer
      - .actual_access:  write_only
        .address_space:  global
        .offset:         80
        .size:           8
        .value_kind:     global_buffer
      - .actual_access:  read_only
        .address_space:  global
        .offset:         88
        .size:           8
        .value_kind:     global_buffer
      - .actual_access:  read_only
        .address_space:  global
        .offset:         96
        .size:           8
        .value_kind:     global_buffer
      - .actual_access:  write_only
        .address_space:  global
        .offset:         104
        .size:           8
        .value_kind:     global_buffer
    .group_segment_fixed_size: 1024
    .kernarg_segment_align: 8
    .kernarg_segment_size: 112
    .language:       OpenCL C
    .language_version:
      - 2
      - 0
    .max_flat_workgroup_size: 1024
    .name:           _Z17prep_count_kernelPKfS0_S0_S0_S0_S0_S0_PDF16_PjPfS1_PKiS5_Pi
    .private_segment_fixed_size: 0
    .sgpr_count:     27
    .sgpr_spill_count: 0
    .symbol:         _Z17prep_count_kernelPKfS0_S0_S0_S0_S0_S0_PDF16_PjPfS1_PKiS5_Pi.kd
    .uniform_work_group_size: 1
    .uses_dynamic_stack: false
    .vgpr_count:     62
    .vgpr_spill_count: 0
    .wavefront_size: 64
  - .agpr_count:     0
    .args:
      - .actual_access:  read_only
        .address_space:  global
        .offset:         0
        .size:           8
        .value_kind:     global_buffer
      - .actual_access:  read_only
        .address_space:  global
        .offset:         8
        .size:           8
        .value_kind:     global_buffer
      - .actual_access:  read_only
        .address_space:  global
        .offset:         16
        .size:           8
        .value_kind:     global_buffer
      - .actual_access:  write_only
        .address_space:  global
        .offset:         24
        .size:           8
        .value_kind:     global_buffer
      - .actual_access:  write_only
        .address_space:  global
        .offset:         32
        .size:           8
        .value_kind:     global_buffer
      - .actual_access:  write_only
        .address_space:  global
        .offset:         40
        .size:           8
        .value_kind:     global_buffer
      - .address_space:  global
        .offset:         48
        .size:           8
        .value_kind:     global_buffer
      - .actual_access:  read_only
        .address_space:  global
        .offset:         56
        .size:           8
        .value_kind:     global_buffer
      - .actual_access:  read_only
        .address_space:  global
        .offset:         64
        .size:           8
        .value_kind:     global_buffer
      - .actual_access:  read_only
        .address_space:  global
        .offset:         72
        .size:           8
        .value_kind:     global_buffer
      - .actual_access:  read_only
        .address_space:  global
        .offset:         80
        .size:           8
        .value_kind:     global_buffer
      - .actual_access:  read_only
        .address_space:  global
        .offset:         88
        .size:           8
        .value_kind:     global_buffer
      - .actual_access:  write_only
        .address_space:  global
        .offset:         96
        .size:           8
        .value_kind:     global_buffer
      - .actual_access:  write_only
        .address_space:  global
        .offset:         104
        .size:           8
        .value_kind:     global_buffer
    .group_segment_fixed_size: 144320
    .kernarg_segment_align: 8
    .kernarg_segment_size: 112
    .language:       OpenCL C
    .language_version:
      - 2
      - 0
    .max_flat_workgroup_size: 512
    .name:           _Z19gemm_scatter_kernelPKfPKDF16_S0_PDF16_S3_PfPjPKiS7_S7_S7_S7_PiS5_
    .private_segment_fixed_size: 0
    .sgpr_count:     46
    .sgpr_spill_count: 0
    .symbol:         _Z19gemm_scatter_kernelPKfPKDF16_S0_PDF16_S3_PfPjPKiS7_S7_S7_S7_PiS5_.kd
    .uniform_work_group_size: 1
    .uses_dynamic_stack: false
    .vgpr_count:     256
    .vgpr_spill_count: 0
    .wavefront_size: 64
  - .agpr_count:     0
    .args:
      - .actual_access:  read_only
        .address_space:  global
        .offset:         0
        .size:           8
        .value_kind:     global_buffer
      - .actual_access:  read_only
        .address_space:  global
        .offset:         8
        .size:           8
        .value_kind:     global_buffer
      - .actual_access:  read_only
        .address_space:  global
        .offset:         16
        .size:           8
        .value_kind:     global_buffer
      - .actual_access:  read_only
        .address_space:  global
        .offset:         24
        .size:           8
        .value_kind:     global_buffer
      - .actual_access:  read_only
        .address_space:  global
        .offset:         32
        .size:           8
        .value_kind:     global_buffer
      - .actual_access:  read_only
        .address_space:  global
        .offset:         40
        .size:           8
        .value_kind:     global_buffer
      - .actual_access:  read_only
        .address_space:  global
        .offset:         48
        .size:           8
        .value_kind:     global_buffer
      - .actual_access:  read_only
        .address_space:  global
        .offset:         56
        .size:           8
        .value_kind:     global_buffer
      - .actual_access:  read_only
        .address_space:  global
        .offset:         64
        .size:           8
        .value_kind:     global_buffer
      - .actual_access:  read_only
        .address_space:  global
        .offset:         72
        .size:           8
        .value_kind:     global_buffer
      - .actual_access:  read_only
        .address_space:  global
        .offset:         80
        .size:           8
        .value_kind:     global_buffer
      - .actual_access:  write_only
        .address_space:  global
        .offset:         88
        .size:           8
        .value_kind:     global_buffer
    .group_segment_fixed_size: 80896
    .kernarg_segment_align: 8
    .kernarg_segment_size: 96
    .language:       OpenCL C
    .language_version:
      - 2
      - 0
    .max_flat_workgroup_size: 1024
    .name:           _Z10agg_kernelPKjPKiPKDF16_S4_PKfS4_S0_S2_S2_S2_S2_Pf
    .private_segment_fixed_size: 0
    .sgpr_count:     78
    .sgpr_spill_count: 0
    .symbol:         _Z10agg_kernelPKjPKiPKDF16_S4_PKfS4_S0_S2_S2_S2_S2_Pf.kd
    .uniform_work_group_size: 1
    .uses_dynamic_stack: false
    .vgpr_count:     64
    .vgpr_spill_count: 0
    .wavefront_size: 64
